# stream hand-structured ring, 14 x 1KiB loads in flight per wave, rotated wave-row assignment
# baseline (speedup 1.0000x reference)
.Lst_nou:
	s_or_b64 exec, exec, s[0:1]
	s_lshr_b32 s8, s3, 6
	v_and_b32_e32 v79, 63, v0
	v_lshlrev_b32_e32 v80, 4, v79
	s_add_i32 s8, s8, s2
	s_and_b32 s8, s8, 15
	s_lshl_b32 s11, s2, 7
	s_lshl_b32 s24, s2, 5
	s_add_i32 s11, s11, s8
	s_lshl_b32 s16, s11, 12
	s_add_i32 s17, s16, 0x10000
	s_add_i32 s18, s16, 0x20000
	s_add_i32 s19, s16, 0x30000
	s_add_i32 s20, s16, 0x40000
	s_add_i32 s21, s16, 0x50000
	s_add_i32 s22, s16, 0x60000
	s_add_i32 s23, s16, 0x70000
	s_waitcnt lgkmcnt(0)
	s_mov_b32 s0, s4
	s_and_b32 s1, s5, 0xffff
	s_brev_b32 s2, 16
	s_mov_b32 s3, 0x20000
	buffer_load_dwordx4 v[16:19], v80, s[0:3], s16 offen nt
	buffer_load_dwordx4 v[20:23], v80, s[0:3], s16 offen offset:1024 nt
	buffer_load_dwordx4 v[24:27], v80, s[0:3], s16 offen offset:2048 nt
	buffer_load_dwordx4 v[28:31], v80, s[0:3], s16 offen offset:3072 nt
	buffer_load_dwordx4 v[32:35], v80, s[0:3], s17 offen nt
	buffer_load_dwordx4 v[36:39], v80, s[0:3], s17 offen offset:1024 nt
	buffer_load_dwordx4 v[40:43], v80, s[0:3], s17 offen offset:2048 nt
	buffer_load_dwordx4 v[44:47], v80, s[0:3], s17 offen offset:3072 nt
	s_barrier
	buffer_load_dwordx4 v[48:51], v80, s[0:3], s18 offen nt
	buffer_load_dwordx4 v[52:55], v80, s[0:3], s18 offen offset:1024 nt
	buffer_load_dwordx4 v[56:59], v80, s[0:3], s18 offen offset:2048 nt
	buffer_load_dwordx4 v[60:63], v80, s[0:3], s18 offen offset:3072 nt
	buffer_load_dwordx4 v[64:67], v80, s[0:3], s19 offen nt
	buffer_load_dwordx4 v[68:71], v80, s[0:3], s19 offen offset:1024 nt
	ds_read_b128 v[0:3], v80
	ds_read_b128 v[4:7], v80 offset:1024
	ds_read_b128 v[8:11], v80 offset:2048
	ds_read_b128 v[12:15], v80 offset:3072
	v_mov_b32_e32 v78, 0
	s_waitcnt lgkmcnt(0)
	s_waitcnt vmcnt(13)
	v_pk_mul_f32 v[72:73], v[16:17], v[0:1]
	v_pk_mul_f32 v[74:75], v[18:19], v[2:3]
	buffer_load_dwordx4 v[16:19], v80, s[0:3], s19 offen offset:2048 nt
	s_waitcnt vmcnt(13)
	v_pk_fma_f32 v[72:73], v[20:21], v[4:5], v[72:73]
	v_pk_fma_f32 v[74:75], v[22:23], v[6:7], v[74:75]
	buffer_load_dwordx4 v[20:23], v80, s[0:3], s19 offen offset:3072 nt
	s_waitcnt vmcnt(13)
	v_pk_fma_f32 v[72:73], v[24:25], v[8:9], v[72:73]
	v_pk_fma_f32 v[74:75], v[26:27], v[10:11], v[74:75]
	buffer_load_dwordx4 v[24:27], v80, s[0:3], s20 offen nt
	s_waitcnt vmcnt(13)
	v_pk_fma_f32 v[72:73], v[28:29], v[12:13], v[72:73]
	v_pk_fma_f32 v[74:75], v[30:31], v[14:15], v[74:75]
	buffer_load_dwordx4 v[28:31], v80, s[0:3], s20 offen offset:1024 nt
	v_pk_add_f32 v[72:73], v[72:73], v[74:75]
	v_cmp_eq_u32_e32 vcc, 0, v79
	v_add_f32_e32 v76, v72, v73
	s_nop 1
	v_add_f32_dpp v76, v76, v76 quad_perm:[1,0,3,2] row_mask:0xf bank_mask:0xf bound_ctrl:1
	s_nop 1
	v_add_f32_dpp v76, v76, v76 quad_perm:[2,3,0,1] row_mask:0xf bank_mask:0xf bound_ctrl:1
	s_nop 1
	v_add_f32_dpp v76, v76, v76 row_ror:4 row_mask:0xf bank_mask:0xf bound_ctrl:1
	s_nop 1
	v_add_f32_dpp v76, v76, v76 row_ror:8 row_mask:0xf bank_mask:0xf bound_ctrl:1
	v_mov_b32_e32 v77, v76
	s_nop 1
	v_permlane16_swap_b32_e32 v76, v77
	v_add_f32_e32 v76, v76, v77
	v_mov_b32_e32 v77, v76
	s_nop 1
	v_permlane32_swap_b32_e32 v76, v77
	v_add_f32_e32 v76, v76, v77
	v_cndmask_b32_e32 v78, v78, v76, vcc
	s_waitcnt vmcnt(13)
	v_pk_mul_f32 v[72:73], v[32:33], v[0:1]
	v_pk_mul_f32 v[74:75], v[34:35], v[2:3]
	buffer_load_dwordx4 v[32:35], v80, s[0:3], s20 offen offset:2048 nt
	s_waitcnt vmcnt(13)
	v_pk_fma_f32 v[72:73], v[36:37], v[4:5], v[72:73]
	v_pk_fma_f32 v[74:75], v[38:39], v[6:7], v[74:75]
	buffer_load_dwordx4 v[36:39], v80, s[0:3], s20 offen offset:3072 nt
	s_waitcnt vmcnt(13)
	v_pk_fma_f32 v[72:73], v[40:41], v[8:9], v[72:73]
	v_pk_fma_f32 v[74:75], v[42:43], v[10:11], v[74:75]
	buffer_load_dwordx4 v[40:43], v80, s[0:3], s21 offen nt
	s_waitcnt vmcnt(13)
	v_pk_fma_f32 v[72:73], v[44:45], v[12:13], v[72:73]
	v_pk_fma_f32 v[74:75], v[46:47], v[14:15], v[74:75]
	buffer_load_dwordx4 v[44:47], v80, s[0:3], s21 offen offset:1024 nt
	v_pk_add_f32 v[72:73], v[72:73], v[74:75]
	v_cmp_eq_u32_e32 vcc, 1, v79
	v_add_f32_e32 v76, v72, v73
	s_nop 1
	v_add_f32_dpp v76, v76, v76 quad_perm:[1,0,3,2] row_mask:0xf bank_mask:0xf bound_ctrl:1
	s_nop 1
	v_add_f32_dpp v76, v76, v76 quad_perm:[2,3,0,1] row_mask:0xf bank_mask:0xf bound_ctrl:1
	s_nop 1
	v_add_f32_dpp v76, v76, v76 row_ror:4 row_mask:0xf bank_mask:0xf bound_ctrl:1
	s_nop 1
	v_add_f32_dpp v76, v76, v76 row_ror:8 row_mask:0xf bank_mask:0xf bound_ctrl:1
	v_mov_b32_e32 v77, v76
	s_nop 1
	v_permlane16_swap_b32_e32 v76, v77
	v_add_f32_e32 v76, v76, v77
	v_mov_b32_e32 v77, v76
	s_nop 1
	v_permlane32_swap_b32_e32 v76, v77
	v_add_f32_e32 v76, v76, v77
	v_cndmask_b32_e32 v78, v78, v76, vcc
	s_waitcnt vmcnt(13)
	v_pk_mul_f32 v[72:73], v[48:49], v[0:1]
	v_pk_mul_f32 v[74:75], v[50:51], v[2:3]
	buffer_load_dwordx4 v[48:51], v80, s[0:3], s21 offen offset:2048 nt
	s_waitcnt vmcnt(13)
	v_pk_fma_f32 v[72:73], v[52:53], v[4:5], v[72:73]
	v_pk_fma_f32 v[74:75], v[54:55], v[6:7], v[74:75]
	buffer_load_dwordx4 v[52:55], v80, s[0:3], s21 offen offset:3072 nt
	s_waitcnt vmcnt(13)
	v_pk_fma_f32 v[72:73], v[56:57], v[8:9], v[72:73]
	v_pk_fma_f32 v[74:75], v[58:59], v[10:11], v[74:75]
	buffer_load_dwordx4 v[56:59], v80, s[0:3], s22 offen nt
	s_waitcnt vmcnt(13)
	v_pk_fma_f32 v[72:73], v[60:61], v[12:13], v[72:73]
	v_pk_fma_f32 v[74:75], v[62:63], v[14:15], v[74:75]
	buffer_load_dwordx4 v[60:63], v80, s[0:3], s22 offen offset:1024 nt
	v_pk_add_f32 v[72:73], v[72:73], v[74:75]
	v_cmp_eq_u32_e32 vcc, 2, v79
	v_add_f32_e32 v76, v72, v73
	s_nop 1
	v_add_f32_dpp v76, v76, v76 quad_perm:[1,0,3,2] row_mask:0xf bank_mask:0xf bound_ctrl:1
	s_nop 1
	v_add_f32_dpp v76, v76, v76 quad_perm:[2,3,0,1] row_mask:0xf bank_mask:0xf bound_ctrl:1
	s_nop 1
	v_add_f32_dpp v76, v76, v76 row_ror:4 row_mask:0xf bank_mask:0xf bound_ctrl:1
	s_nop 1
	v_add_f32_dpp v76, v76, v76 row_ror:8 row_mask:0xf bank_mask:0xf bound_ctrl:1
	v_mov_b32_e32 v77, v76
	s_nop 1
	v_permlane16_swap_b32_e32 v76, v77
	v_add_f32_e32 v76, v76, v77
	v_mov_b32_e32 v77, v76
	s_nop 1
	v_permlane32_swap_b32_e32 v76, v77
	v_add_f32_e32 v76, v76, v77
	v_cndmask_b32_e32 v78, v78, v76, vcc
	s_waitcnt vmcnt(13)
	v_pk_mul_f32 v[72:73], v[64:65], v[0:1]
	v_pk_mul_f32 v[74:75], v[66:67], v[2:3]
	buffer_load_dwordx4 v[64:67], v80, s[0:3], s22 offen offset:2048 nt
	s_waitcnt vmcnt(13)
	v_pk_fma_f32 v[72:73], v[68:69], v[4:5], v[72:73]
	v_pk_fma_f32 v[74:75], v[70:71], v[6:7], v[74:75]
	buffer_load_dwordx4 v[68:71], v80, s[0:3], s22 offen offset:3072 nt
	s_waitcnt vmcnt(13)
	v_pk_fma_f32 v[72:73], v[16:17], v[8:9], v[72:73]
	v_pk_fma_f32 v[74:75], v[18:19], v[10:11], v[74:75]
	buffer_load_dwordx4 v[16:19], v80, s[0:3], s23 offen nt
	s_waitcnt vmcnt(13)
	v_pk_fma_f32 v[72:73], v[20:21], v[12:13], v[72:73]
	v_pk_fma_f32 v[74:75], v[22:23], v[14:15], v[74:75]
	buffer_load_dwordx4 v[20:23], v80, s[0:3], s23 offen offset:1024 nt
	v_pk_add_f32 v[72:73], v[72:73], v[74:75]
	v_cmp_eq_u32_e32 vcc, 3, v79
	v_add_f32_e32 v76, v72, v73
	s_nop 1
	v_add_f32_dpp v76, v76, v76 quad_perm:[1,0,3,2] row_mask:0xf bank_mask:0xf bound_ctrl:1
	s_nop 1
	v_add_f32_dpp v76, v76, v76 quad_perm:[2,3,0,1] row_mask:0xf bank_mask:0xf bound_ctrl:1
	s_nop 1
	v_add_f32_dpp v76, v76, v76 row_ror:4 row_mask:0xf bank_mask:0xf bound_ctrl:1
	s_nop 1
	v_add_f32_dpp v76, v76, v76 row_ror:8 row_mask:0xf bank_mask:0xf bound_ctrl:1
	v_mov_b32_e32 v77, v76
	s_nop 1
	v_permlane16_swap_b32_e32 v76, v77
	v_add_f32_e32 v76, v76, v77
	v_mov_b32_e32 v77, v76
	s_nop 1
	v_permlane32_swap_b32_e32 v76, v77
	v_add_f32_e32 v76, v76, v77
	v_cndmask_b32_e32 v78, v78, v76, vcc
	s_waitcnt vmcnt(13)
	v_pk_mul_f32 v[72:73], v[24:25], v[0:1]
	v_pk_mul_f32 v[74:75], v[26:27], v[2:3]
	buffer_load_dwordx4 v[24:27], v80, s[0:3], s23 offen offset:2048 nt
	s_waitcnt vmcnt(13)
	v_pk_fma_f32 v[72:73], v[28:29], v[4:5], v[72:73]
	v_pk_fma_f32 v[74:75], v[30:31], v[6:7], v[74:75]
	buffer_load_dwordx4 v[28:31], v80, s[0:3], s23 offen offset:3072 nt
	s_waitcnt vmcnt(13)
	v_pk_fma_f32 v[72:73], v[32:33], v[8:9], v[72:73]
	v_pk_fma_f32 v[74:75], v[34:35], v[10:11], v[74:75]
	s_waitcnt vmcnt(12)
	v_pk_fma_f32 v[72:73], v[36:37], v[12:13], v[72:73]
	v_pk_fma_f32 v[74:75], v[38:39], v[14:15], v[74:75]
	s_nop 0
	v_pk_add_f32 v[72:73], v[72:73], v[74:75]
	v_cmp_eq_u32_e32 vcc, 4, v79
	v_add_f32_e32 v76, v72, v73
	s_nop 1
	v_add_f32_dpp v76, v76, v76 quad_perm:[1,0,3,2] row_mask:0xf bank_mask:0xf bound_ctrl:1
	s_nop 1
	v_add_f32_dpp v76, v76, v76 quad_perm:[2,3,0,1] row_mask:0xf bank_mask:0xf bound_ctrl:1
	s_nop 1
	v_add_f32_dpp v76, v76, v76 row_ror:4 row_mask:0xf bank_mask:0xf bound_ctrl:1
	s_nop 1
	v_add_f32_dpp v76, v76, v76 row_ror:8 row_mask:0xf bank_mask:0xf bound_ctrl:1
	v_mov_b32_e32 v77, v76
	s_nop 1
	v_permlane16_swap_b32_e32 v76, v77
	v_add_f32_e32 v76, v76, v77
	v_mov_b32_e32 v77, v76
	s_nop 1
	v_permlane32_swap_b32_e32 v76, v77
	v_add_f32_e32 v76, v76, v77
	v_cndmask_b32_e32 v78, v78, v76, vcc
	s_waitcnt vmcnt(11)
	v_pk_mul_f32 v[72:73], v[40:41], v[0:1]
	v_pk_mul_f32 v[74:75], v[42:43], v[2:3]
	s_waitcnt vmcnt(10)
	v_pk_fma_f32 v[72:73], v[44:45], v[4:5], v[72:73]
	v_pk_fma_f32 v[74:75], v[46:47], v[6:7], v[74:75]
	s_waitcnt vmcnt(9)
	v_pk_fma_f32 v[72:73], v[48:49], v[8:9], v[72:73]
	v_pk_fma_f32 v[74:75], v[50:51], v[10:11], v[74:75]
	s_waitcnt vmcnt(8)
	v_pk_fma_f32 v[72:73], v[52:53], v[12:13], v[72:73]
	v_pk_fma_f32 v[74:75], v[54:55], v[14:15], v[74:75]
	s_nop 0
	v_pk_add_f32 v[72:73], v[72:73], v[74:75]
	v_cmp_eq_u32_e32 vcc, 5, v79
	v_add_f32_e32 v76, v72, v73
	s_nop 1
	v_add_f32_dpp v76, v76, v76 quad_perm:[1,0,3,2] row_mask:0xf bank_mask:0xf bound_ctrl:1
	s_nop 1
	v_add_f32_dpp v76, v76, v76 quad_perm:[2,3,0,1] row_mask:0xf bank_mask:0xf bound_ctrl:1
	s_nop 1
	v_add_f32_dpp v76, v76, v76 row_ror:4 row_mask:0xf bank_mask:0xf bound_ctrl:1
	s_nop 1
	v_add_f32_dpp v76, v76, v76 row_ror:8 row_mask:0xf bank_mask:0xf bound_ctrl:1
	v_mov_b32_e32 v77, v76
	s_nop 1
	v_permlane16_swap_b32_e32 v76, v77
	v_add_f32_e32 v76, v76, v77
	v_mov_b32_e32 v77, v76
	s_nop 1
	v_permlane32_swap_b32_e32 v76, v77
	v_add_f32_e32 v76, v76, v77
	v_cndmask_b32_e32 v78, v78, v76, vcc
	s_waitcnt vmcnt(7)
	v_pk_mul_f32 v[72:73], v[56:57], v[0:1]
	v_pk_mul_f32 v[74:75], v[58:59], v[2:3]
	s_waitcnt vmcnt(6)
	v_pk_fma_f32 v[72:73], v[60:61], v[4:5], v[72:73]
	v_pk_fma_f32 v[74:75], v[62:63], v[6:7], v[74:75]
	s_waitcnt vmcnt(5)
	v_pk_fma_f32 v[72:73], v[64:65], v[8:9], v[72:73]
	v_pk_fma_f32 v[74:75], v[66:67], v[10:11], v[74:75]
	s_waitcnt vmcnt(4)
	v_pk_fma_f32 v[72:73], v[68:69], v[12:13], v[72:73]
	v_pk_fma_f32 v[74:75], v[70:71], v[14:15], v[74:75]
	s_nop 0
	v_pk_add_f32 v[72:73], v[72:73], v[74:75]
	v_cmp_eq_u32_e32 vcc, 6, v79
	v_add_f32_e32 v76, v72, v73
	s_nop 1
	v_add_f32_dpp v76, v76, v76 quad_perm:[1,0,3,2] row_mask:0xf bank_mask:0xf bound_ctrl:1
	s_nop 1
	v_add_f32_dpp v76, v76, v76 quad_perm:[2,3,0,1] row_mask:0xf bank_mask:0xf bound_ctrl:1
	s_nop 1
	v_add_f32_dpp v76, v76, v76 row_ror:4 row_mask:0xf bank_mask:0xf bound_ctrl:1
	s_nop 1
	v_add_f32_dpp v76, v76, v76 row_ror:8 row_mask:0xf bank_mask:0xf bound_ctrl:1
	v_mov_b32_e32 v77, v76
	s_nop 1
	v_permlane16_swap_b32_e32 v76, v77
	v_add_f32_e32 v76, v76, v77
	v_mov_b32_e32 v77, v76
	s_nop 1
	v_permlane32_swap_b32_e32 v76, v77
	v_add_f32_e32 v76, v76, v77
	v_cndmask_b32_e32 v78, v78, v76, vcc
	s_waitcnt vmcnt(3)
	v_pk_mul_f32 v[72:73], v[16:17], v[0:1]
	v_pk_mul_f32 v[74:75], v[18:19], v[2:3]
	s_waitcnt vmcnt(2)
	v_pk_fma_f32 v[72:73], v[20:21], v[4:5], v[72:73]
	v_pk_fma_f32 v[74:75], v[22:23], v[6:7], v[74:75]
	s_waitcnt vmcnt(1)
	v_pk_fma_f32 v[72:73], v[24:25], v[8:9], v[72:73]
	v_pk_fma_f32 v[74:75], v[26:27], v[10:11], v[74:75]
	s_waitcnt vmcnt(0)
	v_pk_fma_f32 v[72:73], v[28:29], v[12:13], v[72:73]
	v_pk_fma_f32 v[74:75], v[30:31], v[14:15], v[74:75]
	s_nop 0
	v_pk_add_f32 v[72:73], v[72:73], v[74:75]
	v_cmp_eq_u32_e32 vcc, 7, v79
	v_add_f32_e32 v76, v72, v73
	s_nop 1
	v_add_f32_dpp v76, v76, v76 quad_perm:[1,0,3,2] row_mask:0xf bank_mask:0xf bound_ctrl:1
	s_nop 1
	v_add_f32_dpp v76, v76, v76 quad_perm:[2,3,0,1] row_mask:0xf bank_mask:0xf bound_ctrl:1
	s_nop 1
	v_add_f32_dpp v76, v76, v76 row_ror:4 row_mask:0xf bank_mask:0xf bound_ctrl:1
	s_nop 1
	v_add_f32_dpp v76, v76, v76 row_ror:8 row_mask:0xf bank_mask:0xf bound_ctrl:1
	v_mov_b32_e32 v77, v76
	s_nop 1
	v_permlane16_swap_b32_e32 v76, v77
	v_add_f32_e32 v76, v76, v77
	v_mov_b32_e32 v77, v76
	s_nop 1
	v_permlane32_swap_b32_e32 v76, v77
	v_add_f32_e32 v76, v76, v77
	v_cndmask_b32_e32 v78, v78, v76, vcc
	v_cmp_gt_u32_e32 vcc, 8, v79
	s_and_saveexec_b64 s[0:1], vcc
	v_lshlrev_b32_e32 v77, 2, v79
	s_lshl_b32 s9, s8, 13
	s_add_i32 s9, s9, s24
	s_addk_i32 s9, 0x6040
	v_add_u32_e32 v77, s9, v77
	global_store_dword v77, v78, s[6:7]
	s_endpgm

	.amdhsa_kernel _Z13stream_kernelPKfPf
		.amdhsa_group_segment_fixed_size 4096
		.amdhsa_private_segment_fixed_size 0
		.amdhsa_kernarg_size 16
		.amdhsa_user_sgpr_count 2
		.amdhsa_user_sgpr_dispatch_ptr 0
		.amdhsa_user_sgpr_queue_ptr 0
		.amdhsa_user_sgpr_kernarg_segment_ptr 1
		.amdhsa_user_sgpr_dispatch_id 0
		.amdhsa_user_sgpr_kernarg_preload_length 0
		.amdhsa_user_sgpr_kernarg_preload_offset 0
		.amdhsa_user_sgpr_private_segment_size 0
		.amdhsa_uses_dynamic_stack 0
		.amdhsa_enable_private_segment 0
		.amdhsa_system_sgpr_workgroup_id_x 1
		.amdhsa_system_sgpr_workgroup_id_y 0
		.amdhsa_system_sgpr_workgroup_id_z 0
		.amdhsa_system_sgpr_workgroup_info 0
		.amdhsa_system_vgpr_workitem_id 0
		.amdhsa_next_free_vgpr 81
		.amdhsa_next_free_sgpr 25
		.amdhsa_accum_offset 84
		.amdhsa_reserve_vcc 1
		.amdhsa_float_round_mode_32 0
		.amdhsa_float_round_mode_16_64 0
		.amdhsa_float_denorm_mode_32 3
		.amdhsa_float_denorm_mode_16_64 3
		.amdhsa_dx10_clamp 1
		.amdhsa_ieee_mode 1
		.amdhsa_fp16_overflow 0
		.amdhsa_tg_split 0
		.amdhsa_exception_fp_ieee_invalid_op 0
		.amdhsa_exception_fp_denorm_src 0
		.amdhsa_exception_fp_ieee_div_zero 0
		.amdhsa_exception_fp_ieee_overflow 0
		.amdhsa_exception_fp_ieee_underflow 0
		.amdhsa_exception_fp_ieee_inexact 0
		.amdhsa_exception_int_div_zero 0
	.end_amdhsa_kernel

.Lfunc_end1:
	.size	_Z13stream_kernelPKfPf, .Lfunc_end1-_Z13stream_kernelPKfPf
	.set _Z13stream_kernelPKfPf.num_vgpr, 81
	.set _Z13stream_kernelPKfPf.num_agpr, 0
	.set _Z13stream_kernelPKfPf.numbered_sgpr, 25
	.set _Z13stream_kernelPKfPf.num_named_barrier, 0
	.set _Z13stream_kernelPKfPf.private_seg_size, 0
	.set _Z13stream_kernelPKfPf.uses_vcc, 1
	.set _Z13stream_kernelPKfPf.uses_flat_scratch, 0
	.set _Z13stream_kernelPKfPf.has_dyn_sized_stack, 0
	.set _Z13stream_kernelPKfPf.has_recursion, 0
	.set _Z13stream_kernelPKfPf.has_indirect_call, 0

amdhsa.kernels:
  - .agpr_count:     0
    .args:
      - .actual_access:  read_only
        .address_space:  global
        .offset:         0
        .size:           8
        .value_kind:     global_buffer
      - .actual_access:  read_only
        .address_space:  global
        .offset:         8
        .size:           8
        .value_kind:     global_buffer
      - .actual_access:  read_only
        .address_space:  global
        .offset:         16
        .size:           8
        .value_kind:     global_buffer
      - .actual_access:  read_only
        .address_space:  global
        .offset:         24
        .size:           8
        .value_kind:     global_buffer
      - .actual_access:  write_only
        .address_space:  global
        .offset:         32
        .size:           8
        .value_kind:     global_buffer
    .group_segment_fixed_size: 2112
    .kernarg_segment_align: 8
    .kernarg_segment_size: 40
    .language:       OpenCL C
    .language_version:
      - 2
      - 0
    .max_flat_workgroup_size: 1024
    .name:           _Z11prep_kernelPKfS0_S0_S0_Pf
    .private_segment_fixed_size: 0
    .sgpr_count:     32
    .sgpr_spill_count: 0
    .symbol:         _Z11prep_kernelPKfS0_S0_S0_Pf.kd
    .uniform_work_group_size: 1
    .uses_dynamic_stack: false
    .vgpr_count:     40
    .vgpr_spill_count: 0
    .wavefront_size: 64
  - .agpr_count:     0
    .args:
      - .actual_access:  read_only
        .address_space:  global
        .offset:         0
        .size:           8
        .value_kind:     global_buffer
      - .address_space:  global
        .offset:         8
        .size:           8
        .value_kind:     global_buffer
    .group_segment_fixed_size: 4096
    .kernarg_segment_align: 8
    .kernarg_segment_size: 16
    .language:       OpenCL C
    .language_version:
      - 2
      - 0
    .max_flat_workgroup_size: 1024
    .name:           _Z13stream_kernelPKfPf
    .private_segment_fixed_size: 0
    .sgpr_count:     31
    .sgpr_spill_count: 0
    .symbol:         _Z13stream_kernelPKfPf.kd
    .uniform_work_group_size: 1
    .uses_dynamic_stack: false
    .vgpr_count:     81
    .vgpr_spill_count: 0
    .wavefront_size: 64
  - .agpr_count:     0
    .args:
      - .actual_access:  read_only
        .address_space:  global
        .offset:         0
        .size:           8
        .value_kind:     global_buffer
      - .actual_access:  write_only
        .address_space:  global
        .offset:         8
        .size:           8
        .value_kind:     global_buffer
    .group_segment_fixed_size: 32
    .kernarg_segment_align: 8
    .kernarg_segment_size: 16
    .language:       OpenCL C
    .language_version:
      - 2
      - 0
    .max_flat_workgroup_size: 256
    .name:           _Z14softmax_kernelPKfPf
    .private_segment_fixed_size: 0
    .sgpr_count:     16
    .sgpr_spill_count: 0
    .symbol:         _Z14softmax_kernelPKfPf.kd
    .uniform_work_group_size: 1
    .uses_dynamic_stack: false
    .vgpr_count:     17
    .vgpr_spill_count: 0
    .wavefront_size: 64
